# P19 final norm: g_final chunks preloaded once per lane instead of load+vmcnt(0)+store per chunk per row
# baseline (speedup 1.0000x reference)
;     __device__ __forceinline__ const float* x() const { return (const float*)ld(0); }
;     __device__ __forceinline__ const float* c() const { return (const float*)ld(1); }
;     __device__ __forceinline__ const float* g_final() const { return (const float*)ld(24); }
;     __device__ __forceinline__ unsigned char* ws() const { return (unsigned char*)ld(26); }
; __device__ __forceinline__ void combine_phase(const Ctx& a, int layer, int G) {
;     ...
;     _Float16* X = (_Float16*)(a.ws() + WS_X); const bf16_t* Y = (const bf16_t*)(a.ws() + WS_Y); const int* POS = (const int*)(a.ws() + WS_POS);
;     const float* modl = (const float*)(a.ws() + WS_MODL);
;     const float* gf = modl + layer * 12288 + 5 * DM;
;     const int gw = blockIdx.x * NWAVES + wave, NGW = G * NWAVES;
;     int pl[4]; f16x4 nx[4][8];
; #pragma unroll
;     for (int i = 0; i < 4; ++i) { const int row = gw + i * NGW; pl[i] = -1;
;         if (row < SEQ) { pl[i] = (lane < NE) ? POS[(size_t)lane * SEQ + row] : -1;
; #pragma unroll
;             for (int j = 0; j < 8; ++j) nx[i][j] = *(const f16x4*)(X + (size_t)row * DM + ((j >> 1) * 512 + lane * 8 + (j & 1) * 4)); } }
;     ...
;             for (int j = 0; j < 8; ++j) { const int c = ((j >> 1) * 512 + lane * 8 + (j & 1) * 4); *(f32x4*)(orow + c) = v[j] * rstd * *(const f32x4*)(a.g_final() + c); }
.LBB0_2235:
	s_lshl_b32 s17, s20, 4
	s_add_u32 s2, s4, 0x26000
	v_mov_b32_e32 v25, 0
	s_addc_u32 s3, s5, 0
	v_lshlrev_b32_e32 v4, 2, v94
	v_mov_b32_e32 v5, v25
	v_or_b32_e32 v26, 0x400, v94
	v_lshl_add_u64 v[98:99], s[2:3], 0, v[4:5]
	v_or_b32_e32 v4, 0x800, v4
	v_or_b32_e32 v30, 0x600, v94
	v_lshl_add_u64 v[100:101], s[2:3], 0, v[4:5]
	v_lshlrev_b32_e32 v4, 2, v26
	v_lshl_add_u64 v[102:103], s[2:3], 0, v[4:5]
	v_lshlrev_b32_e32 v4, 2, v30
	s_add_i32 s19, 0, 0x23f00
	v_lshl_add_u64 v[104:105], s[2:3], 0, v[4:5]
	v_mov_b32_e32 v4, s19
	ds_read_b128 v[4:7], v4
	v_lshlrev_b32_e32 v24, 1, v94
	v_or_b32_e32 v28, 0x404, v94
	v_or_b32_e32 v32, 0x604, v94
	v_lshl_add_u64 v[96:97], s[6:7], 0, v[24:25]
	v_lshl_add_u64 v[24:25], s[4:5], 0, v[24:25]
	s_mov_b64 s[2:3], 0x2f9d0000
	s_mul_i32 s16, s20, 24
	s_lshl_b32 s18, s20, 5
	v_lshl_add_u64 v[106:107], v[24:25], 0, s[2:3]
	s_mulk_i32 s20, 0xffe8
	v_mov_b32_e32 v95, 0x358637bd
	s_mov_b32 s21, 0xf800000
	v_mov_b32_e32 v140, 0x260
	v_lshlrev_b32_e32 v141, 2, v26
	v_lshlrev_b32_e32 v142, 2, v28
	v_lshlrev_b32_e32 v143, 2, v30
	v_lshlrev_b32_e32 v144, 2, v32
	s_waitcnt lgkmcnt(0)
	v_readfirstlane_b32 s98, v4
	v_readfirstlane_b32 s99, v5
	v_lshlrev_b32_e32 v215, 2, v94
	v_add_u32_e32 v200, 0x1000, v215
	s_nop 3
	global_load_dwordx4 v[216:219], v215, s[98:99]
	global_load_dwordx4 v[220:223], v215, s[98:99] offset:16
	global_load_dwordx4 v[224:227], v215, s[98:99] offset:2048
	global_load_dwordx4 v[228:231], v215, s[98:99] offset:2064
	global_load_dwordx4 v[232:235], v200, s[98:99]
	global_load_dwordx4 v[236:239], v200, s[98:99] offset:16
	global_load_dwordx4 v[240:243], v200, s[98:99] offset:2048
	global_load_dwordx4 v[244:247], v200, s[98:99] offset:2064
	s_waitcnt vmcnt(4)
	v_mov_b32_e32 v145, v84
	s_branch .LBB0_2239

;     __device__ __forceinline__ const float* x() const { return (const float*)ld(0); }
;     __device__ __forceinline__ const float* c() const { return (const float*)ld(1); }
; __device__ __forceinline__ void combine_phase(const Ctx& a, int layer, int G) {
;     ...
;       for (int i = 0; i < 4; ++i) { const int row = base + i * NGW;
;        if (row < SEQ) {
;         _Float16* xr = X + (size_t)row * DM; f32x4 v[8], sum[8];
;         const int plc = pl[i]; unsigned long long sel = __ballot(plc >= 0);
; #pragma unroll
;         for (int j = 0; j < 8; ++j) { v[j] = __builtin_convertvector(nx[i][j], f32x4); sum[j] = (f32x4){0.f, 0.f, 0.f, 0.f}; }
;         { const int nrow = row + 4 * NGW;
;           if (nrow < SEQ) { pl[i] = (lane < NE) ? POS[(size_t)lane * SEQ + nrow] : -1;
; #pragma unroll
;             for (int j = 0; j < 8; ++j) nx[i][j] = *(const f16x4*)(X + (size_t)nrow * DM + ((j >> 1) * 512 + lane * 8 + (j & 1) * 4)); } }
;         while (sel) { const int e0 = __builtin_ctzll(sel); sel &= sel - 1;
;             const bf16_t* y0 = Y + (size_t)(e0 * CAP + __builtin_amdgcn_readlane(plc, e0)) * DM;
;             u32x2 w0[8];
; #pragma unroll
;             for (int j = 0; j < 8; ++j) w0[j] = *(const u32x2*)(y0 + ((j >> 1) * 512 + lane * 8 + (j & 1) * 4));
; #pragma unroll
;             for (int j = 0; j < 8; ++j) sum[j] += (f32x4){bflo(w0[j].x), bfhi(w0[j].x), bflo(w0[j].y), bfhi(w0[j].y)}; }
;         float ss = 0.f;
; #pragma unroll
;         for (int j = 0; j < 8; ++j) { const int c = ((j >> 1) * 512 + lane * 8 + (j & 1) * 4); v[j] = v[j] + *(const f32x4*)(gf + c) * sum[j];
;             ss += (v[j].x * v[j].x + v[j].y * v[j].y) + (v[j].z * v[j].z + v[j].w * v[j].w); }
.LBB0_2237:
	global_load_dwordx4 v[88:91], v[98:99], off
	global_load_dwordx4 v[84:87], v[98:99], off offset:16
	global_load_dwordx4 v[152:155], v[100:101], off
	global_load_dwordx4 v[156:159], v[100:101], off offset:16
	global_load_dwordx4 v[160:163], v[102:103], off
	global_load_dwordx4 v[164:167], v[102:103], off offset:16
	global_load_dwordx4 v[168:171], v[104:105], off offset:16
	global_load_dwordx4 v[172:175], v[104:105], off
	v_cvt_f32_f16_sdwa v185, v60 dst_sel:DWORD dst_unused:UNUSED_PAD src0_sel:WORD_1
	v_cvt_f32_f16_sdwa v187, v61 dst_sel:DWORD dst_unused:UNUSED_PAD src0_sel:WORD_1
	v_cvt_f32_f16_e32 v184, v60
	v_cvt_f32_f16_e32 v186, v61
	v_cvt_f32_f16_sdwa v61, v62 dst_sel:DWORD dst_unused:UNUSED_PAD src0_sel:WORD_1
	v_cvt_f32_f16_sdwa v189, v63 dst_sel:DWORD dst_unused:UNUSED_PAD src0_sel:WORD_1
	v_cvt_f32_f16_e32 v60, v62
	v_cvt_f32_f16_e32 v188, v63
	v_cvt_f32_f16_sdwa v63, v64 dst_sel:DWORD dst_unused:UNUSED_PAD src0_sel:WORD_1
	v_cvt_f32_f16_sdwa v191, v65 dst_sel:DWORD dst_unused:UNUSED_PAD src0_sel:WORD_1
	v_cvt_f32_f16_e32 v62, v64
	v_cvt_f32_f16_e32 v190, v65
	v_cvt_f32_f16_sdwa v65, v66 dst_sel:DWORD dst_unused:UNUSED_PAD src0_sel:WORD_1
	v_cvt_f32_f16_sdwa v193, v67 dst_sel:DWORD dst_unused:UNUSED_PAD src0_sel:WORD_1
	v_cvt_f32_f16_e32 v64, v66
	v_cvt_f32_f16_e32 v192, v67
	v_cvt_f32_f16_sdwa v67, v52 dst_sel:DWORD dst_unused:UNUSED_PAD src0_sel:WORD_1
	v_cvt_f32_f16_e32 v66, v52
	v_mov_b32_e32 v52, s19
	v_cvt_f32_f16_sdwa v177, v56 dst_sel:DWORD dst_unused:UNUSED_PAD src0_sel:WORD_1
	v_cvt_f32_f16_sdwa v179, v57 dst_sel:DWORD dst_unused:UNUSED_PAD src0_sel:WORD_1
	v_cvt_f32_f16_e32 v176, v56
	v_cvt_f32_f16_e32 v178, v57
	v_cvt_f32_f16_sdwa v181, v58 dst_sel:DWORD dst_unused:UNUSED_PAD src0_sel:WORD_1
	v_cvt_f32_f16_sdwa v183, v59 dst_sel:DWORD dst_unused:UNUSED_PAD src0_sel:WORD_1
	v_cvt_f32_f16_e32 v180, v58
	v_cvt_f32_f16_e32 v182, v59
	ds_read_b128 v[56:59], v52
	v_cvt_f32_f16_sdwa v195, v53 dst_sel:DWORD dst_unused:UNUSED_PAD src0_sel:WORD_1
	v_cvt_f32_f16_e32 v194, v53
	v_cvt_f32_f16_sdwa v197, v54 dst_sel:DWORD dst_unused:UNUSED_PAD src0_sel:WORD_1
	v_cvt_f32_f16_sdwa v199, v55 dst_sel:DWORD dst_unused:UNUSED_PAD src0_sel:WORD_1
	s_waitcnt lgkmcnt(0)
	v_readfirstlane_b32 s11, v57
	v_readfirstlane_b32 s10, v56
	v_cvt_f32_f16_e32 v196, v54
	v_cvt_f32_f16_e32 v198, v55
	s_ashr_i32 s9, s8, 31
	v_readfirstlane_b32 s12, v58
	v_readfirstlane_b32 s5, v59
	global_load_dwordx4 v[52:55], v149, s[10:11]
	s_waitcnt vmcnt(13)
	v_mov_b32_e32 v148, v150
	s_waitcnt vmcnt(8)
	v_pk_fma_f32 v[56:57], v[138:139], v[90:91], v[178:179]
	v_pk_fma_f32 v[88:89], v[136:137], v[88:89], v[176:177]
	s_waitcnt vmcnt(7)
	v_pk_fma_f32 v[86:87], v[134:135], v[86:87], v[182:183]
	v_pk_fma_f32 v[84:85], v[132:133], v[84:85], v[180:181]
	s_waitcnt vmcnt(6)
	v_pk_fma_f32 v[90:91], v[130:131], v[154:155], v[186:187]
	v_pk_fma_f32 v[128:129], v[128:129], v[152:153], v[184:185]
	s_waitcnt vmcnt(4)
	v_pk_fma_f32 v[62:63], v[120:121], v[160:161], v[62:63]
	s_waitcnt vmcnt(3)
	v_pk_fma_f32 v[64:65], v[116:117], v[164:165], v[64:65]
	v_mul_f32_e32 v116, v89, v89
	v_mul_f32_e32 v117, v57, v57
	v_mul_f32_e32 v120, v85, v85
	v_mul_f32_e32 v121, v87, v87
	v_pk_fma_f32 v[126:127], v[126:127], v[158:159], v[188:189]
	v_pk_fma_f32 v[60:61], v[124:125], v[156:157], v[60:61]
	v_mul_f32_e32 v124, v129, v129
	v_mul_f32_e32 v125, v91, v91
	v_fmac_f32_e32 v116, v88, v88
	v_fmac_f32_e32 v117, v56, v56
	v_fmac_f32_e32 v120, v84, v84
	v_fmac_f32_e32 v121, v86, v86
	v_pk_fma_f32 v[122:123], v[122:123], v[162:163], v[190:191]
	v_mul_f32_e32 v130, v61, v61
	v_mul_f32_e32 v131, v127, v127
	v_fmac_f32_e32 v124, v128, v128
	v_fmac_f32_e32 v125, v90, v90
	v_add_f32_e32 v116, v116, v117
	v_add_f32_e32 v117, v120, v121
	v_pk_fma_f32 v[118:119], v[118:119], v[166:167], v[192:193]
	v_mul_f32_e32 v132, v63, v63
	v_mul_f32_e32 v133, v123, v123
	v_fmac_f32_e32 v130, v60, v60
	v_fmac_f32_e32 v131, v126, v126
	v_add_f32_e32 v120, v124, v125
	v_add_f32_e32 v116, v116, v117
	v_mul_f32_e32 v134, v65, v65
	v_fmac_f32_e32 v132, v62, v62
	v_fmac_f32_e32 v133, v122, v122
	v_add_f32_e32 v121, v130, v131
	v_add_f32_e32 v116, v116, v120
	v_mul_f32_e32 v117, v119, v119
	s_waitcnt vmcnt(1)
;     __device__ __forceinline__ const float* x() const { return (const float*)ld(0); }
;     __device__ __forceinline__ const float* c() const { return (const float*)ld(1); }
;     __device__ __forceinline__ const float* g_final() const { return (const float*)ld(24); }
;     __device__ __forceinline__ float* out() const { return (float*)ld(25); }
; __device__ __forceinline__ void combine_phase(const Ctx& a, int layer, int G) {
;     ...
;         for (int j = 0; j < 8; ++j) { const int c = ((j >> 1) * 512 + lane * 8 + (j & 1) * 4); v[j] = v[j] + *(const f32x4*)(gf + c) * sum[j];
;             ss += (v[j].x * v[j].x + v[j].y * v[j].y) + (v[j].z * v[j].z + v[j].w * v[j].w); }
;         const float rstd = 1.0f / sqrtf(wave_sum(ss) * (1.0f / DM) + EPS);
;     ...
;             float* orow = a.out() + (size_t)row * DM;
; #pragma unroll
;             for (int j = 0; j < 8; ++j) { const int c = ((j >> 1) * 512 + lane * 8 + (j & 1) * 4); *(f32x4*)(orow + c) = v[j] * rstd * *(const f32x4*)(a.g_final() + c); }
	v_pk_fma_f32 v[114:115], v[114:115], v[174:175], v[194:195]
	v_pk_fma_f32 v[66:67], v[112:113], v[172:173], v[66:67]
	v_fmac_f32_e32 v134, v64, v64
	v_add_f32_e32 v124, v132, v133
	v_add_f32_e32 v116, v116, v121
	v_fmac_f32_e32 v117, v118, v118
	v_mul_f32_e32 v112, v67, v67
	v_mul_f32_e32 v113, v115, v115
	v_add_f32_e32 v116, v116, v124
	v_add_f32_e32 v117, v134, v117
	v_fmac_f32_e32 v112, v66, v66
	v_fmac_f32_e32 v113, v114, v114
	v_add_f32_e32 v116, v116, v117
	v_add_f32_e32 v112, v112, v113
	v_pk_fma_f32 v[110:111], v[110:111], v[170:171], v[198:199]
	v_pk_fma_f32 v[108:109], v[108:109], v[168:169], v[196:197]
	v_add_f32_e32 v112, v116, v112
	v_mul_f32_e32 v113, v109, v109
	v_mul_f32_e32 v116, v111, v111
	v_fmac_f32_e32 v113, v108, v108
	v_fmac_f32_e32 v116, v110, v110
	v_add_f32_e32 v113, v113, v116
	v_add_f32_e32 v112, v112, v113
	s_nop 1
	v_add_f32_dpp v112, v112, v112 quad_perm:[1,0,3,2] row_mask:0xf bank_mask:0xf bound_ctrl:1
	s_nop 1
	v_add_f32_dpp v112, v112, v112 quad_perm:[2,3,0,1] row_mask:0xf bank_mask:0xf bound_ctrl:1
	s_nop 1
	v_add_f32_dpp v112, v112, v112 row_half_mirror row_mask:0xf bank_mask:0xf bound_ctrl:1
	s_nop 1
	v_add_f32_dpp v112, v112, v112 row_mirror row_mask:0xf bank_mask:0xf bound_ctrl:1
	v_mov_b32_e32 v113, v112
	s_nop 1
	v_permlane16_swap_b32_e32 v112, v113
	v_add_f32_e32 v112, v112, v113
	v_mov_b32_e32 v113, v112
	s_nop 1
	v_permlane32_swap_b32_e32 v112, v113
	v_add_f32_e32 v112, v112, v113
	v_fmamk_f32 v112, v112, 0x3a000000, v95
	v_mul_f32_e32 v113, 0x4f800000, v112
	v_cmp_gt_f32_e32 vcc, s21, v112
	s_nop 1
	v_cndmask_b32_e32 v112, v112, v113, vcc
	v_sqrt_f32_e32 v113, v112
	s_nop 0
	v_add_u32_e32 v116, -1, v113
	v_fma_f32 v117, -v116, v113, v112
	v_cmp_ge_f32_e64 s[2:3], 0, v117
	v_add_u32_e32 v117, 1, v113
	s_nop 0
	v_cndmask_b32_e64 v116, v113, v116, s[2:3]
	v_fma_f32 v113, -v117, v113, v112
	v_cmp_lt_f32_e64 s[2:3], 0, v113
	s_nop 1
	v_cndmask_b32_e64 v113, v116, v117, s[2:3]
	v_mul_f32_e32 v116, 0x37800000, v113
	v_cndmask_b32_e32 v113, v113, v116, vcc
	v_cmp_class_f32_e32 vcc, v112, v140
	s_nop 1
	v_cndmask_b32_e32 v112, v113, v112, vcc
	v_div_scale_f32 v113, s[2:3], v112, v112, 1.0
	v_rcp_f32_e32 v116, v113
	s_lshl_b64 s[2:3], s[8:9], 13
	s_add_u32 s2, s12, s2
	s_addc_u32 s3, s5, s3
	v_fma_f32 v117, -v113, v116, 1.0
	v_fmac_f32_e32 v116, v117, v116
	v_div_scale_f32 v117, vcc, 1.0, v112, 1.0
	v_mul_f32_e32 v120, v117, v116
	v_fma_f32 v121, -v113, v120, v117
	v_fmac_f32_e32 v120, v121, v116
	v_fma_f32 v113, -v113, v120, v117
	v_div_fmas_f32 v113, v113, v116, v120
	v_div_fixup_f32 v112, v113, v112, 1.0
	v_pk_mul_f32 v[58:59], v[88:89], v[112:113] op_sel_hi:[1,0]
	v_pk_mul_f32 v[56:57], v[56:57], v[112:113] op_sel_hi:[1,0]
	s_waitcnt vmcnt(0)
	v_pk_mul_f32 v[52:53], v[52:53], v[58:59]
	v_pk_mul_f32 v[54:55], v[54:55], v[56:57]
	global_store_dwordx4 v149, v[52:55], s[2:3]
	v_pk_mul_f32 v[56:57], v[86:87], v[112:113] op_sel_hi:[1,0]
	v_pk_mul_f32 v[58:59], v[84:85], v[112:113] op_sel_hi:[1,0]
	v_pk_mul_f32 v[54:55], v[222:223], v[56:57]
	v_pk_mul_f32 v[52:53], v[220:221], v[58:59]
	global_store_dwordx4 v149, v[52:55], s[2:3] offset:16
	v_pk_mul_f32 v[56:57], v[90:91], v[112:113] op_sel_hi:[1,0]
	v_pk_mul_f32 v[58:59], v[128:129], v[112:113] op_sel_hi:[1,0]
	v_pk_mul_f32 v[54:55], v[226:227], v[56:57]
	v_pk_mul_f32 v[52:53], v[224:225], v[58:59]
	global_store_dwordx4 v149, v[52:55], s[2:3] offset:2048
	v_pk_mul_f32 v[56:57], v[126:127], v[112:113] op_sel_hi:[1,0]
	v_pk_mul_f32 v[58:59], v[60:61], v[112:113] op_sel_hi:[1,0]
	v_mov_b64_e32 v[60:61], v[72:73]
	v_pk_mul_f32 v[52:53], v[58:59], v[228:229]
	v_pk_mul_f32 v[54:55], v[56:57], v[230:231]
	global_store_dwordx4 v149, v[52:55], s[2:3] offset:2064
	v_pk_mul_f32 v[56:57], v[122:123], v[112:113] op_sel_hi:[1,0]
	v_pk_mul_f32 v[58:59], v[62:63], v[112:113] op_sel_hi:[1,0]
	v_mov_b64_e32 v[62:63], v[74:75]
	v_pk_mul_f32 v[52:53], v[58:59], v[232:233]
	v_pk_mul_f32 v[54:55], v[56:57], v[234:235]
	global_store_dwordx4 v141, v[52:55], s[2:3]
	v_pk_mul_f32 v[56:57], v[118:119], v[112:113] op_sel_hi:[1,0]
	v_pk_mul_f32 v[58:59], v[64:65], v[112:113] op_sel_hi:[1,0]
	v_mov_b64_e32 v[64:65], v[76:77]
	v_pk_mul_f32 v[52:53], v[58:59], v[236:237]
	v_pk_mul_f32 v[54:55], v[56:57], v[238:239]
	global_store_dwordx4 v142, v[52:55], s[2:3]
	v_pk_mul_f32 v[56:57], v[114:115], v[112:113] op_sel_hi:[1,0]
	v_pk_mul_f32 v[58:59], v[66:67], v[112:113] op_sel_hi:[1,0]
	v_mov_b64_e32 v[66:67], v[78:79]
	v_pk_mul_f32 v[52:53], v[58:59], v[240:241]
	v_pk_mul_f32 v[54:55], v[56:57], v[242:243]
	global_store_dwordx4 v143, v[52:55], s[2:3]
	v_mov_b64_e32 v[56:57], v[68:69]
	v_mov_b64_e32 v[58:59], v[70:71]
	v_pk_mul_f32 v[70:71], v[110:111], v[112:113] op_sel_hi:[1,0]
	v_pk_mul_f32 v[68:69], v[108:109], v[112:113] op_sel_hi:[1,0]
	v_mov_b64_e32 v[52:53], v[80:81]
	v_mov_b64_e32 v[54:55], v[82:83]
	v_pk_mul_f32 v[68:69], v[68:69], v[244:245]
	v_pk_mul_f32 v[70:71], v[70:71], v[246:247]
	global_store_dwordx4 v144, v[68:71], s[2:3]

;     __device__ __forceinline__ const float* x() const { return (const float*)ld(0); }
;     __device__ __forceinline__ const float* c() const { return (const float*)ld(1); }
; __device__ __forceinline__ void combine_phase(const Ctx& a, int layer, int G) {
;     ...
;       for (int i = 0; i < 4; ++i) { const int row = base + i * NGW;
;        if (row < SEQ) {
;         _Float16* xr = X + (size_t)row * DM; f32x4 v[8], sum[8];
;         const int plc = pl[i]; unsigned long long sel = __ballot(plc >= 0);
; #pragma unroll
;         for (int j = 0; j < 8; ++j) { v[j] = __builtin_convertvector(nx[i][j], f32x4); sum[j] = (f32x4){0.f, 0.f, 0.f, 0.f}; }
;         { const int nrow = row + 4 * NGW;
;           if (nrow < SEQ) { pl[i] = (lane < NE) ? POS[(size_t)lane * SEQ + nrow] : -1;
; #pragma unroll
;             for (int j = 0; j < 8; ++j) nx[i][j] = *(const f16x4*)(X + (size_t)nrow * DM + ((j >> 1) * 512 + lane * 8 + (j & 1) * 4)); } }
;         while (sel) { const int e0 = __builtin_ctzll(sel); sel &= sel - 1;
;             const bf16_t* y0 = Y + (size_t)(e0 * CAP + __builtin_amdgcn_readlane(plc, e0)) * DM;
;             u32x2 w0[8];
; #pragma unroll
;             for (int j = 0; j < 8; ++j) w0[j] = *(const u32x2*)(y0 + ((j >> 1) * 512 + lane * 8 + (j & 1) * 4));
; #pragma unroll
;             for (int j = 0; j < 8; ++j) sum[j] += (f32x4){bflo(w0[j].x), bfhi(w0[j].x), bflo(w0[j].y), bfhi(w0[j].y)}; }
;         float ss = 0.f;
; #pragma unroll
;         for (int j = 0; j < 8; ++j) { const int c = ((j >> 1) * 512 + lane * 8 + (j & 1) * 4); v[j] = v[j] + *(const f32x4*)(gf + c) * sum[j];
;             ss += (v[j].x * v[j].x + v[j].y * v[j].y) + (v[j].z * v[j].z + v[j].w * v[j].w); }
.LBB0_2247:
	global_load_dwordx4 v[88:91], v[98:99], off
	global_load_dwordx4 v[84:87], v[98:99], off offset:16
	global_load_dwordx4 v[150:153], v[100:101], off
	global_load_dwordx4 v[154:157], v[100:101], off offset:16
	global_load_dwordx4 v[158:161], v[102:103], off
	global_load_dwordx4 v[162:165], v[102:103], off offset:16
	global_load_dwordx4 v[166:169], v[104:105], off offset:16
	global_load_dwordx4 v[170:173], v[104:105], off
	s_waitcnt lgkmcnt(0)
	v_readfirstlane_b32 s11, v5
	v_readfirstlane_b32 s10, v4
	v_lshlrev_b32_e32 v149, 2, v94
	v_cvt_f32_f16_sdwa v175, v80 dst_sel:DWORD dst_unused:UNUSED_PAD src0_sel:WORD_1
	v_cvt_f32_f16_sdwa v177, v81 dst_sel:DWORD dst_unused:UNUSED_PAD src0_sel:WORD_1
	v_cvt_f32_f16_e32 v174, v80
	v_cvt_f32_f16_e32 v176, v81
	v_cvt_f32_f16_sdwa v81, v82 dst_sel:DWORD dst_unused:UNUSED_PAD src0_sel:WORD_1
	v_cvt_f32_f16_sdwa v179, v83 dst_sel:DWORD dst_unused:UNUSED_PAD src0_sel:WORD_1
	v_cvt_f32_f16_e32 v80, v82
	v_cvt_f32_f16_e32 v178, v83
	v_cvt_f32_f16_sdwa v83, v76 dst_sel:DWORD dst_unused:UNUSED_PAD src0_sel:WORD_1
	v_cvt_f32_f16_sdwa v181, v77 dst_sel:DWORD dst_unused:UNUSED_PAD src0_sel:WORD_1
	v_cvt_f32_f16_e32 v82, v76
	v_cvt_f32_f16_e32 v180, v77
	v_cvt_f32_f16_sdwa v77, v78 dst_sel:DWORD dst_unused:UNUSED_PAD src0_sel:WORD_1
	v_cvt_f32_f16_sdwa v183, v79 dst_sel:DWORD dst_unused:UNUSED_PAD src0_sel:WORD_1
	v_cvt_f32_f16_e32 v76, v78
	v_cvt_f32_f16_e32 v182, v79
	v_cvt_f32_f16_sdwa v79, v72 dst_sel:DWORD dst_unused:UNUSED_PAD src0_sel:WORD_1
	v_cvt_f32_f16_sdwa v185, v73 dst_sel:DWORD dst_unused:UNUSED_PAD src0_sel:WORD_1
	v_cvt_f32_f16_e32 v78, v72
	v_cvt_f32_f16_e32 v184, v73
	v_cvt_f32_f16_sdwa v73, v74 dst_sel:DWORD dst_unused:UNUSED_PAD src0_sel:WORD_1
	v_cvt_f32_f16_sdwa v187, v75 dst_sel:DWORD dst_unused:UNUSED_PAD src0_sel:WORD_1
	v_cvt_f32_f16_e32 v72, v74
	v_cvt_f32_f16_e32 v186, v75
	v_cvt_f32_f16_sdwa v75, v68 dst_sel:DWORD dst_unused:UNUSED_PAD src0_sel:WORD_1
	v_cvt_f32_f16_sdwa v189, v69 dst_sel:DWORD dst_unused:UNUSED_PAD src0_sel:WORD_1
	v_cvt_f32_f16_e32 v74, v68
	v_cvt_f32_f16_e32 v188, v69
	v_cvt_f32_f16_sdwa v191, v70 dst_sel:DWORD dst_unused:UNUSED_PAD src0_sel:WORD_1
	v_cvt_f32_f16_sdwa v193, v71 dst_sel:DWORD dst_unused:UNUSED_PAD src0_sel:WORD_1
	v_cvt_f32_f16_e32 v190, v70
	v_cvt_f32_f16_e32 v192, v71
	global_load_dwordx4 v[68:71], v149, s[10:11]
	s_ashr_i32 s9, s8, 31
	v_readfirstlane_b32 s12, v6
	v_readfirstlane_b32 s5, v7
	s_waitcnt vmcnt(8)
	v_pk_fma_f32 v[90:91], v[138:139], v[90:91], v[176:177]
	v_pk_fma_f32 v[88:89], v[136:137], v[88:89], v[174:175]
	s_waitcnt vmcnt(7)
	v_pk_fma_f32 v[86:87], v[134:135], v[86:87], v[178:179]
	v_pk_fma_f32 v[80:81], v[132:133], v[84:85], v[80:81]
	s_waitcnt vmcnt(6)
	v_pk_fma_f32 v[84:85], v[130:131], v[152:153], v[180:181]
	v_pk_fma_f32 v[82:83], v[128:129], v[150:151], v[82:83]
	s_waitcnt vmcnt(4)
	v_pk_fma_f32 v[78:79], v[120:121], v[158:159], v[78:79]
	s_waitcnt vmcnt(3)
	v_pk_fma_f32 v[72:73], v[116:117], v[162:163], v[72:73]
	v_mul_f32_e32 v116, v89, v89
	v_mul_f32_e32 v117, v91, v91
	v_mul_f32_e32 v120, v81, v81
	v_mul_f32_e32 v121, v87, v87
	v_pk_fma_f32 v[126:127], v[126:127], v[156:157], v[182:183]
	v_pk_fma_f32 v[76:77], v[124:125], v[154:155], v[76:77]
	v_mul_f32_e32 v124, v83, v83
	v_mul_f32_e32 v125, v85, v85
	v_fmac_f32_e32 v116, v88, v88
	v_fmac_f32_e32 v117, v90, v90
	v_fmac_f32_e32 v120, v80, v80
	v_fmac_f32_e32 v121, v86, v86
	v_pk_fma_f32 v[122:123], v[122:123], v[160:161], v[184:185]
	v_mul_f32_e32 v128, v77, v77
	v_mul_f32_e32 v129, v127, v127
	v_fmac_f32_e32 v124, v82, v82
	v_fmac_f32_e32 v125, v84, v84
	v_add_f32_e32 v116, v116, v117
	v_add_f32_e32 v117, v120, v121
	v_pk_fma_f32 v[118:119], v[118:119], v[164:165], v[186:187]
	v_mul_f32_e32 v130, v79, v79
	v_mul_f32_e32 v131, v123, v123
	v_fmac_f32_e32 v128, v76, v76
	v_fmac_f32_e32 v129, v126, v126
	v_add_f32_e32 v120, v124, v125
	v_add_f32_e32 v116, v116, v117
	v_mul_f32_e32 v132, v73, v73
	v_mul_f32_e32 v133, v119, v119
	v_fmac_f32_e32 v130, v78, v78
	v_fmac_f32_e32 v131, v122, v122
	v_add_f32_e32 v121, v128, v129
	v_add_f32_e32 v116, v116, v120
	s_waitcnt vmcnt(1)
;     __device__ __forceinline__ const float* x() const { return (const float*)ld(0); }
;     __device__ __forceinline__ const float* c() const { return (const float*)ld(1); }
;     __device__ __forceinline__ const float* g_final() const { return (const float*)ld(24); }
;     __device__ __forceinline__ float* out() const { return (float*)ld(25); }
; __device__ __forceinline__ void combine_phase(const Ctx& a, int layer, int G) {
;     ...
;     for (int base = gw; base < SEQ; base += 4 * NGW) {
; #pragma unroll
;       for (int i = 0; i < 4; ++i) { const int row = base + i * NGW;
;        if (row < SEQ) {
;         _Float16* xr = X + (size_t)row * DM; f32x4 v[8], sum[8];
;         const int plc = pl[i]; unsigned long long sel = __ballot(plc >= 0);
; #pragma unroll
;         for (int j = 0; j < 8; ++j) { v[j] = __builtin_convertvector(nx[i][j], f32x4); sum[j] = (f32x4){0.f, 0.f, 0.f, 0.f}; }
;         { const int nrow = row + 4 * NGW;
;           if (nrow < SEQ) { pl[i] = (lane < NE) ? POS[(size_t)lane * SEQ + nrow] : -1;
; #pragma unroll
;             for (int j = 0; j < 8; ++j) nx[i][j] = *(const f16x4*)(X + (size_t)nrow * DM + ((j >> 1) * 512 + lane * 8 + (j & 1) * 4)); } }
;     ...
;         for (int j = 0; j < 8; ++j) { const int c = ((j >> 1) * 512 + lane * 8 + (j & 1) * 4); v[j] = v[j] + *(const f32x4*)(gf + c) * sum[j];
;             ss += (v[j].x * v[j].x + v[j].y * v[j].y) + (v[j].z * v[j].z + v[j].w * v[j].w); }
;         const float rstd = 1.0f / sqrtf(wave_sum(ss) * (1.0f / DM) + EPS);
;     ...
;             float* orow = a.out() + (size_t)row * DM;
; #pragma unroll
;             for (int j = 0; j < 8; ++j) { const int c = ((j >> 1) * 512 + lane * 8 + (j & 1) * 4); *(f32x4*)(orow + c) = v[j] * rstd * *(const f32x4*)(a.g_final() + c); }
	v_pk_fma_f32 v[114:115], v[114:115], v[172:173], v[188:189]
	v_pk_fma_f32 v[74:75], v[112:113], v[170:171], v[74:75]
	v_fmac_f32_e32 v132, v72, v72
	v_add_f32_e32 v124, v130, v131
	v_add_f32_e32 v116, v116, v121
	v_fmac_f32_e32 v133, v118, v118
	v_mul_f32_e32 v112, v75, v75
	v_mul_f32_e32 v113, v115, v115
	v_add_f32_e32 v116, v116, v124
	v_add_f32_e32 v117, v132, v133
	v_fmac_f32_e32 v112, v74, v74
	v_fmac_f32_e32 v113, v114, v114
	v_add_f32_e32 v116, v116, v117
	v_add_f32_e32 v112, v112, v113
	v_pk_fma_f32 v[110:111], v[110:111], v[168:169], v[192:193]
	v_pk_fma_f32 v[108:109], v[108:109], v[166:167], v[190:191]
	v_add_f32_e32 v112, v116, v112
	v_mul_f32_e32 v113, v109, v109
	v_mul_f32_e32 v116, v111, v111
	v_fmac_f32_e32 v113, v108, v108
	v_fmac_f32_e32 v116, v110, v110
	v_add_f32_e32 v113, v113, v116
	v_add_f32_e32 v112, v112, v113
	s_nop 1
	v_add_f32_dpp v112, v112, v112 quad_perm:[1,0,3,2] row_mask:0xf bank_mask:0xf bound_ctrl:1
	s_nop 1
	v_add_f32_dpp v112, v112, v112 quad_perm:[2,3,0,1] row_mask:0xf bank_mask:0xf bound_ctrl:1
	s_nop 1
	v_add_f32_dpp v112, v112, v112 row_half_mirror row_mask:0xf bank_mask:0xf bound_ctrl:1
	s_nop 1
	v_add_f32_dpp v112, v112, v112 row_mirror row_mask:0xf bank_mask:0xf bound_ctrl:1
	v_mov_b32_e32 v113, v112
	s_nop 1
	v_permlane16_swap_b32_e32 v112, v113
	v_add_f32_e32 v112, v112, v113
	v_mov_b32_e32 v113, v112
	s_nop 1
	v_permlane32_swap_b32_e32 v112, v113
	v_add_f32_e32 v112, v112, v113
	v_fmamk_f32 v112, v112, 0x3a000000, v95
	v_mul_f32_e32 v113, 0x4f800000, v112
	v_cmp_gt_f32_e32 vcc, s21, v112
	s_nop 1
	v_cndmask_b32_e32 v112, v112, v113, vcc
	v_sqrt_f32_e32 v113, v112
	s_nop 0
	v_add_u32_e32 v116, -1, v113
	v_fma_f32 v117, -v116, v113, v112
	v_cmp_ge_f32_e64 s[2:3], 0, v117
	v_add_u32_e32 v117, 1, v113
	s_nop 0
	v_cndmask_b32_e64 v116, v113, v116, s[2:3]
	v_fma_f32 v113, -v117, v113, v112
	v_cmp_lt_f32_e64 s[2:3], 0, v113
	s_nop 1
	v_cndmask_b32_e64 v113, v116, v117, s[2:3]
	v_mul_f32_e32 v116, 0x37800000, v113
	v_cndmask_b32_e32 v113, v113, v116, vcc
	v_cmp_class_f32_e32 vcc, v112, v140
	s_nop 1
	v_cndmask_b32_e32 v112, v113, v112, vcc
	v_div_scale_f32 v113, s[2:3], v112, v112, 1.0
	v_rcp_f32_e32 v116, v113
	s_lshl_b64 s[2:3], s[8:9], 13
	s_add_u32 s2, s12, s2
	s_addc_u32 s3, s5, s3
	v_fma_f32 v117, -v113, v116, 1.0
	v_fmac_f32_e32 v116, v117, v116
	v_div_scale_f32 v117, vcc, 1.0, v112, 1.0
	v_mul_f32_e32 v120, v117, v116
	v_fma_f32 v121, -v113, v120, v117
	v_fmac_f32_e32 v120, v121, v116
	v_fma_f32 v113, -v113, v120, v117
	v_div_fmas_f32 v113, v113, v116, v120
	v_div_fixup_f32 v112, v113, v112, 1.0
	v_pk_mul_f32 v[88:89], v[88:89], v[112:113] op_sel_hi:[1,0]
	v_pk_mul_f32 v[90:91], v[90:91], v[112:113] op_sel_hi:[1,0]
	s_waitcnt vmcnt(0)
	v_pk_mul_f32 v[68:69], v[68:69], v[88:89]
	v_pk_mul_f32 v[70:71], v[70:71], v[90:91]
	global_store_dwordx4 v149, v[68:71], s[2:3]
	v_pk_mul_f32 v[86:87], v[86:87], v[112:113] op_sel_hi:[1,0]
	v_pk_mul_f32 v[80:81], v[80:81], v[112:113] op_sel_hi:[1,0]
	v_pk_mul_f32 v[82:83], v[82:83], v[112:113] op_sel_hi:[1,0]
	v_pk_mul_f32 v[76:77], v[76:77], v[112:113] op_sel_hi:[1,0]
	v_pk_mul_f32 v[78:79], v[78:79], v[112:113] op_sel_hi:[1,0]
	v_pk_mul_f32 v[72:73], v[72:73], v[112:113] op_sel_hi:[1,0]
	v_pk_mul_f32 v[74:75], v[74:75], v[112:113] op_sel_hi:[1,0]
	v_pk_mul_f32 v[68:69], v[220:221], v[80:81]
	v_pk_mul_f32 v[70:71], v[222:223], v[86:87]
	global_store_dwordx4 v149, v[68:71], s[2:3] offset:16
	s_nop 0
	v_pk_mul_f32 v[80:81], v[84:85], v[112:113] op_sel_hi:[1,0]
	v_pk_mul_f32 v[68:69], v[224:225], v[82:83]
	v_pk_mul_f32 v[70:71], v[226:227], v[80:81]
	global_store_dwordx4 v149, v[68:71], s[2:3] offset:2048
	s_nop 0
	v_pk_mul_f32 v[80:81], v[126:127], v[112:113] op_sel_hi:[1,0]
	v_pk_mul_f32 v[68:69], v[76:77], v[228:229]
	v_pk_mul_f32 v[70:71], v[80:81], v[230:231]
	global_store_dwordx4 v149, v[68:71], s[2:3] offset:2064
	s_nop 0
	v_pk_mul_f32 v[76:77], v[122:123], v[112:113] op_sel_hi:[1,0]
	v_pk_mul_f32 v[68:69], v[78:79], v[232:233]
	v_pk_mul_f32 v[70:71], v[76:77], v[234:235]
	global_store_dwordx4 v141, v[68:71], s[2:3]
	s_nop 0
	v_pk_mul_f32 v[76:77], v[118:119], v[112:113] op_sel_hi:[1,0]
	v_pk_mul_f32 v[68:69], v[72:73], v[236:237]
	v_pk_mul_f32 v[70:71], v[76:77], v[238:239]
	global_store_dwordx4 v142, v[68:71], s[2:3]
	s_nop 0
	v_pk_mul_f32 v[72:73], v[114:115], v[112:113] op_sel_hi:[1,0]
	v_pk_mul_f32 v[68:69], v[74:75], v[240:241]
	v_pk_mul_f32 v[70:71], v[72:73], v[242:243]
	global_store_dwordx4 v143, v[68:71], s[2:3]
	s_add_i32 s10, s4, s20
	v_pk_mul_f32 v[72:73], v[110:111], v[112:113] op_sel_hi:[1,0]
	v_pk_mul_f32 v[74:75], v[108:109], v[112:113] op_sel_hi:[1,0]
	s_cmpk_lt_i32 s10, 0x2000
	v_pk_mul_f32 v[68:69], v[74:75], v[244:245]
	v_pk_mul_f32 v[70:71], v[72:73], v[246:247]
	global_store_dwordx4 v144, v[68:71], s[2:3]
	s_cbranch_scc0 .LBB0_2255
	s_add_i32 s12, s10, s18
	v_cmp_lt_i32_e64 s[2:3], -1, v146
	s_cmpk_gt_i32 s12, 0x1fff
	v_mov_b64_e32 v[68:69], v[8:9]
	v_mov_b64_e32 v[70:71], v[10:11]
	v_mov_b64_e32 v[72:73], v[12:13]
	v_mov_b64_e32 v[74:75], v[14:15]
	v_mov_b64_e32 v[76:77], v[16:17]
	v_mov_b64_e32 v[78:79], v[18:19]
	v_mov_b64_e32 v[80:81], v[0:1]
	v_mov_b64_e32 v[82:83], v[2:3]
	v_mov_b32_e32 v150, v146
	s_cbranch_scc1 .LBB0_2252
	s_ashr_i32 s13, s12, 31
	v_mov_b32_e32 v150, -1
	s_and_saveexec_b64 s[14:15], s[0:1]
	s_cbranch_execz .LBB0_2251
	v_lshl_add_u64 v[68:69], s[12:13], 2, v[92:93]
	global_load_dword v150, v[68:69], off

;     __device__ __forceinline__ const float* x() const { return (const float*)ld(0); }
;     __device__ __forceinline__ const float* c() const { return (const float*)ld(1); }
; __device__ __forceinline__ void combine_phase(const Ctx& a, int layer, int G) {
;     ...
;       for (int i = 0; i < 4; ++i) { const int row = base + i * NGW;
;        if (row < SEQ) {
;         _Float16* xr = X + (size_t)row * DM; f32x4 v[8], sum[8];
;         const int plc = pl[i]; unsigned long long sel = __ballot(plc >= 0);
; #pragma unroll
;         for (int j = 0; j < 8; ++j) { v[j] = __builtin_convertvector(nx[i][j], f32x4); sum[j] = (f32x4){0.f, 0.f, 0.f, 0.f}; }
;         { const int nrow = row + 4 * NGW;
;           if (nrow < SEQ) { pl[i] = (lane < NE) ? POS[(size_t)lane * SEQ + nrow] : -1;
; #pragma unroll
;             for (int j = 0; j < 8; ++j) nx[i][j] = *(const f16x4*)(X + (size_t)nrow * DM + ((j >> 1) * 512 + lane * 8 + (j & 1) * 4)); } }
;         while (sel) { const int e0 = __builtin_ctzll(sel); sel &= sel - 1;
;             const bf16_t* y0 = Y + (size_t)(e0 * CAP + __builtin_amdgcn_readlane(plc, e0)) * DM;
;             u32x2 w0[8];
; #pragma unroll
;             for (int j = 0; j < 8; ++j) w0[j] = *(const u32x2*)(y0 + ((j >> 1) * 512 + lane * 8 + (j & 1) * 4));
; #pragma unroll
;             for (int j = 0; j < 8; ++j) sum[j] += (f32x4){bflo(w0[j].x), bfhi(w0[j].x), bflo(w0[j].y), bfhi(w0[j].y)}; }
;         float ss = 0.f;
; #pragma unroll
;         for (int j = 0; j < 8; ++j) { const int c = ((j >> 1) * 512 + lane * 8 + (j & 1) * 4); v[j] = v[j] + *(const f32x4*)(gf + c) * sum[j];
;             ss += (v[j].x * v[j].x + v[j].y * v[j].y) + (v[j].z * v[j].z + v[j].w * v[j].w); }
.LBB0_2264:
	global_load_dwordx4 v[88:91], v[98:99], off
	global_load_dwordx4 v[84:87], v[98:99], off offset:16
	global_load_dwordx4 v[152:155], v[100:101], off
	global_load_dwordx4 v[156:159], v[100:101], off offset:16
	global_load_dwordx4 v[160:163], v[102:103], off
	global_load_dwordx4 v[164:167], v[102:103], off offset:16
	global_load_dwordx4 v[168:171], v[104:105], off offset:16
	global_load_dwordx4 v[172:175], v[104:105], off
	v_cvt_f32_f16_sdwa v185, v12 dst_sel:DWORD dst_unused:UNUSED_PAD src0_sel:WORD_1
	v_cvt_f32_f16_sdwa v187, v13 dst_sel:DWORD dst_unused:UNUSED_PAD src0_sel:WORD_1
	v_cvt_f32_f16_e32 v184, v12
	v_cvt_f32_f16_e32 v186, v13
	v_cvt_f32_f16_sdwa v13, v14 dst_sel:DWORD dst_unused:UNUSED_PAD src0_sel:WORD_1
	v_cvt_f32_f16_sdwa v189, v15 dst_sel:DWORD dst_unused:UNUSED_PAD src0_sel:WORD_1
	v_cvt_f32_f16_e32 v12, v14
	v_cvt_f32_f16_e32 v188, v15
	v_cvt_f32_f16_sdwa v15, v16 dst_sel:DWORD dst_unused:UNUSED_PAD src0_sel:WORD_1
	v_cvt_f32_f16_sdwa v191, v17 dst_sel:DWORD dst_unused:UNUSED_PAD src0_sel:WORD_1
	v_cvt_f32_f16_e32 v14, v16
	v_cvt_f32_f16_e32 v190, v17
	v_cvt_f32_f16_sdwa v17, v18 dst_sel:DWORD dst_unused:UNUSED_PAD src0_sel:WORD_1
	v_cvt_f32_f16_sdwa v193, v19 dst_sel:DWORD dst_unused:UNUSED_PAD src0_sel:WORD_1
	v_cvt_f32_f16_e32 v16, v18
	v_cvt_f32_f16_e32 v192, v19
	v_cvt_f32_f16_sdwa v19, v0 dst_sel:DWORD dst_unused:UNUSED_PAD src0_sel:WORD_1
	v_cvt_f32_f16_e32 v18, v0
	v_mov_b32_e32 v0, s19
	v_cvt_f32_f16_sdwa v177, v8 dst_sel:DWORD dst_unused:UNUSED_PAD src0_sel:WORD_1
	v_cvt_f32_f16_sdwa v179, v9 dst_sel:DWORD dst_unused:UNUSED_PAD src0_sel:WORD_1
	v_cvt_f32_f16_e32 v176, v8
	v_cvt_f32_f16_e32 v178, v9
	v_cvt_f32_f16_sdwa v181, v10 dst_sel:DWORD dst_unused:UNUSED_PAD src0_sel:WORD_1
	v_cvt_f32_f16_sdwa v183, v11 dst_sel:DWORD dst_unused:UNUSED_PAD src0_sel:WORD_1
	v_cvt_f32_f16_e32 v180, v10
	v_cvt_f32_f16_e32 v182, v11
	ds_read_b128 v[8:11], v0
	v_cvt_f32_f16_sdwa v195, v1 dst_sel:DWORD dst_unused:UNUSED_PAD src0_sel:WORD_1
	v_cvt_f32_f16_e32 v194, v1
	v_cvt_f32_f16_sdwa v197, v2 dst_sel:DWORD dst_unused:UNUSED_PAD src0_sel:WORD_1
	v_cvt_f32_f16_sdwa v199, v3 dst_sel:DWORD dst_unused:UNUSED_PAD src0_sel:WORD_1
	s_waitcnt lgkmcnt(0)
	v_readfirstlane_b32 s13, v9
	v_readfirstlane_b32 s12, v8
	v_cvt_f32_f16_e32 v196, v2
	v_cvt_f32_f16_e32 v198, v3
	s_ashr_i32 s11, s10, 31
	v_readfirstlane_b32 s9, v10
	v_readfirstlane_b32 s5, v11
	global_load_dwordx4 v[0:3], v149, s[12:13]
	s_waitcnt vmcnt(13)
	v_mov_b32_e32 v146, v150
	s_waitcnt vmcnt(8)
	v_pk_fma_f32 v[8:9], v[138:139], v[90:91], v[178:179]
	v_pk_fma_f32 v[88:89], v[136:137], v[88:89], v[176:177]
	s_waitcnt vmcnt(7)
	v_pk_fma_f32 v[86:87], v[134:135], v[86:87], v[182:183]
	v_pk_fma_f32 v[84:85], v[132:133], v[84:85], v[180:181]
	s_waitcnt vmcnt(6)
	v_pk_fma_f32 v[90:91], v[130:131], v[154:155], v[186:187]
	v_pk_fma_f32 v[128:129], v[128:129], v[152:153], v[184:185]
	s_waitcnt vmcnt(4)
	v_pk_fma_f32 v[14:15], v[120:121], v[160:161], v[14:15]
	s_waitcnt vmcnt(3)
	v_pk_fma_f32 v[16:17], v[116:117], v[164:165], v[16:17]
	v_mul_f32_e32 v116, v89, v89
	v_mul_f32_e32 v117, v9, v9
	v_mul_f32_e32 v120, v85, v85
	v_mul_f32_e32 v121, v87, v87
	v_pk_fma_f32 v[126:127], v[126:127], v[158:159], v[188:189]
	v_pk_fma_f32 v[12:13], v[124:125], v[156:157], v[12:13]
	v_mul_f32_e32 v124, v129, v129
	v_mul_f32_e32 v125, v91, v91
	v_fmac_f32_e32 v116, v88, v88
	v_fmac_f32_e32 v117, v8, v8
	v_fmac_f32_e32 v120, v84, v84
	v_fmac_f32_e32 v121, v86, v86
	v_pk_fma_f32 v[122:123], v[122:123], v[162:163], v[190:191]
	v_mul_f32_e32 v130, v13, v13
	v_mul_f32_e32 v131, v127, v127
	v_fmac_f32_e32 v124, v128, v128
	v_fmac_f32_e32 v125, v90, v90
	v_add_f32_e32 v116, v116, v117
	v_add_f32_e32 v117, v120, v121
	v_pk_fma_f32 v[118:119], v[118:119], v[166:167], v[192:193]
	v_mul_f32_e32 v132, v15, v15
	v_mul_f32_e32 v133, v123, v123
	v_fmac_f32_e32 v130, v12, v12
	v_fmac_f32_e32 v131, v126, v126
	v_add_f32_e32 v120, v124, v125
	v_add_f32_e32 v116, v116, v117
	v_mul_f32_e32 v134, v17, v17
	v_fmac_f32_e32 v132, v14, v14
	v_fmac_f32_e32 v133, v122, v122
	v_add_f32_e32 v121, v130, v131
	v_add_f32_e32 v116, v116, v120
	v_mul_f32_e32 v117, v119, v119
	s_waitcnt vmcnt(1)
;     __device__ __forceinline__ const float* x() const { return (const float*)ld(0); }
;     __device__ __forceinline__ const float* c() const { return (const float*)ld(1); }
;     __device__ __forceinline__ const float* g_final() const { return (const float*)ld(24); }
;     __device__ __forceinline__ float* out() const { return (float*)ld(25); }
; __device__ __forceinline__ void combine_phase(const Ctx& a, int layer, int G) {
;     ...
;         for (int j = 0; j < 8; ++j) { const int c = ((j >> 1) * 512 + lane * 8 + (j & 1) * 4); v[j] = v[j] + *(const f32x4*)(gf + c) * sum[j];
;             ss += (v[j].x * v[j].x + v[j].y * v[j].y) + (v[j].z * v[j].z + v[j].w * v[j].w); }
;         const float rstd = 1.0f / sqrtf(wave_sum(ss) * (1.0f / DM) + EPS);
;     ...
;             float* orow = a.out() + (size_t)row * DM;
; #pragma unroll
;             for (int j = 0; j < 8; ++j) { const int c = ((j >> 1) * 512 + lane * 8 + (j & 1) * 4); *(f32x4*)(orow + c) = v[j] * rstd * *(const f32x4*)(a.g_final() + c); }
	v_pk_fma_f32 v[114:115], v[114:115], v[174:175], v[194:195]
	v_pk_fma_f32 v[18:19], v[112:113], v[172:173], v[18:19]
	v_fmac_f32_e32 v134, v16, v16
	v_add_f32_e32 v124, v132, v133
	v_add_f32_e32 v116, v116, v121
	v_fmac_f32_e32 v117, v118, v118
	v_mul_f32_e32 v112, v19, v19
	v_mul_f32_e32 v113, v115, v115
	v_add_f32_e32 v116, v116, v124
	v_add_f32_e32 v117, v134, v117
	v_fmac_f32_e32 v112, v18, v18
	v_fmac_f32_e32 v113, v114, v114
	v_add_f32_e32 v116, v116, v117
	v_add_f32_e32 v112, v112, v113
	v_pk_fma_f32 v[110:111], v[110:111], v[170:171], v[198:199]
	v_pk_fma_f32 v[108:109], v[108:109], v[168:169], v[196:197]
	v_add_f32_e32 v112, v116, v112
	v_mul_f32_e32 v113, v109, v109
	v_mul_f32_e32 v116, v111, v111
	v_fmac_f32_e32 v113, v108, v108
	v_fmac_f32_e32 v116, v110, v110
	v_add_f32_e32 v113, v113, v116
	v_add_f32_e32 v112, v112, v113
	s_nop 1
	v_add_f32_dpp v112, v112, v112 quad_perm:[1,0,3,2] row_mask:0xf bank_mask:0xf bound_ctrl:1
	s_nop 1
	v_add_f32_dpp v112, v112, v112 quad_perm:[2,3,0,1] row_mask:0xf bank_mask:0xf bound_ctrl:1
	s_nop 1
	v_add_f32_dpp v112, v112, v112 row_half_mirror row_mask:0xf bank_mask:0xf bound_ctrl:1
	s_nop 1
	v_add_f32_dpp v112, v112, v112 row_mirror row_mask:0xf bank_mask:0xf bound_ctrl:1
	v_mov_b32_e32 v113, v112
	s_nop 1
	v_permlane16_swap_b32_e32 v112, v113
	v_add_f32_e32 v112, v112, v113
	v_mov_b32_e32 v113, v112
	s_nop 1
	v_permlane32_swap_b32_e32 v112, v113
	v_add_f32_e32 v112, v112, v113
	v_fmamk_f32 v112, v112, 0x3a000000, v95
	v_mul_f32_e32 v113, 0x4f800000, v112
	v_cmp_gt_f32_e32 vcc, s21, v112
	s_nop 1
	v_cndmask_b32_e32 v112, v112, v113, vcc
	v_sqrt_f32_e32 v113, v112
	s_nop 0
	v_add_u32_e32 v116, -1, v113
	v_fma_f32 v117, -v116, v113, v112
	v_cmp_ge_f32_e64 s[2:3], 0, v117
	v_add_u32_e32 v117, 1, v113
	s_nop 0
	v_cndmask_b32_e64 v116, v113, v116, s[2:3]
	v_fma_f32 v113, -v117, v113, v112
	v_cmp_lt_f32_e64 s[2:3], 0, v113
	s_nop 1
	v_cndmask_b32_e64 v113, v116, v117, s[2:3]
	v_mul_f32_e32 v116, 0x37800000, v113
	v_cndmask_b32_e32 v113, v113, v116, vcc
	v_cmp_class_f32_e32 vcc, v112, v140
	s_nop 1
	v_cndmask_b32_e32 v112, v113, v112, vcc
	v_div_scale_f32 v113, s[2:3], v112, v112, 1.0
	v_rcp_f32_e32 v116, v113
	s_lshl_b64 s[2:3], s[10:11], 13
	s_add_u32 s2, s9, s2
	s_addc_u32 s3, s5, s3
	v_fma_f32 v117, -v113, v116, 1.0
	v_fmac_f32_e32 v116, v117, v116
	v_div_scale_f32 v117, vcc, 1.0, v112, 1.0
	v_mul_f32_e32 v120, v117, v116
	v_fma_f32 v121, -v113, v120, v117
	v_fmac_f32_e32 v120, v121, v116
	v_fma_f32 v113, -v113, v120, v117
	v_div_fmas_f32 v113, v113, v116, v120
	v_div_fixup_f32 v112, v113, v112, 1.0
	v_pk_mul_f32 v[10:11], v[88:89], v[112:113] op_sel_hi:[1,0]
	v_pk_mul_f32 v[8:9], v[8:9], v[112:113] op_sel_hi:[1,0]
	s_waitcnt vmcnt(0)
	v_pk_mul_f32 v[0:1], v[0:1], v[10:11]
	v_pk_mul_f32 v[2:3], v[2:3], v[8:9]
	global_store_dwordx4 v149, v[0:3], s[2:3]
	v_pk_mul_f32 v[8:9], v[86:87], v[112:113] op_sel_hi:[1,0]
	v_pk_mul_f32 v[10:11], v[84:85], v[112:113] op_sel_hi:[1,0]
	v_pk_mul_f32 v[2:3], v[222:223], v[8:9]
	v_pk_mul_f32 v[0:1], v[220:221], v[10:11]
	global_store_dwordx4 v149, v[0:3], s[2:3] offset:16
	v_pk_mul_f32 v[8:9], v[90:91], v[112:113] op_sel_hi:[1,0]
	v_pk_mul_f32 v[10:11], v[128:129], v[112:113] op_sel_hi:[1,0]
	v_pk_mul_f32 v[2:3], v[226:227], v[8:9]
	v_pk_mul_f32 v[0:1], v[224:225], v[10:11]
	global_store_dwordx4 v149, v[0:3], s[2:3] offset:2048
	v_pk_mul_f32 v[8:9], v[126:127], v[112:113] op_sel_hi:[1,0]
	v_pk_mul_f32 v[10:11], v[12:13], v[112:113] op_sel_hi:[1,0]
	v_mov_b64_e32 v[12:13], v[72:73]
	v_pk_mul_f32 v[0:1], v[10:11], v[228:229]
	v_pk_mul_f32 v[2:3], v[8:9], v[230:231]
	global_store_dwordx4 v149, v[0:3], s[2:3] offset:2064
	v_pk_mul_f32 v[8:9], v[122:123], v[112:113] op_sel_hi:[1,0]
	v_pk_mul_f32 v[10:11], v[14:15], v[112:113] op_sel_hi:[1,0]
	v_mov_b64_e32 v[14:15], v[74:75]
	v_pk_mul_f32 v[0:1], v[10:11], v[232:233]
	v_pk_mul_f32 v[2:3], v[8:9], v[234:235]
	global_store_dwordx4 v141, v[0:3], s[2:3]
	v_pk_mul_f32 v[8:9], v[118:119], v[112:113] op_sel_hi:[1,0]
	v_pk_mul_f32 v[10:11], v[16:17], v[112:113] op_sel_hi:[1,0]
	v_mov_b64_e32 v[16:17], v[76:77]
	v_pk_mul_f32 v[0:1], v[10:11], v[236:237]
	v_pk_mul_f32 v[2:3], v[8:9], v[238:239]
	global_store_dwordx4 v142, v[0:3], s[2:3]
	v_pk_mul_f32 v[8:9], v[114:115], v[112:113] op_sel_hi:[1,0]
	v_pk_mul_f32 v[10:11], v[18:19], v[112:113] op_sel_hi:[1,0]
	v_mov_b64_e32 v[18:19], v[78:79]
	v_pk_mul_f32 v[0:1], v[10:11], v[240:241]
	v_pk_mul_f32 v[2:3], v[8:9], v[242:243]
	global_store_dwordx4 v143, v[0:3], s[2:3]
	v_mov_b64_e32 v[8:9], v[68:69]
	v_mov_b64_e32 v[10:11], v[70:71]
	v_pk_mul_f32 v[70:71], v[110:111], v[112:113] op_sel_hi:[1,0]
	v_pk_mul_f32 v[68:69], v[108:109], v[112:113] op_sel_hi:[1,0]
	v_mov_b64_e32 v[0:1], v[80:81]
	v_mov_b64_e32 v[2:3], v[82:83]
	v_pk_mul_f32 v[68:69], v[68:69], v[244:245]
	v_pk_mul_f32 v[70:71], v[70:71], v[246:247]
	global_store_dwordx4 v144, v[68:71], s[2:3]
	s_add_i32 s10, s8, s17
	s_cmpk_gt_i32 s10, 0x1fff
	s_cbranch_scc0 .LBB0_2256

;     __device__ __forceinline__ const float* x() const { return (const float*)ld(0); }
;     __device__ __forceinline__ const float* c() const { return (const float*)ld(1); }
; __device__ __forceinline__ void combine_phase(const Ctx& a, int layer, int G) {
;     ...
;       for (int i = 0; i < 4; ++i) { const int row = base + i * NGW;
;        if (row < SEQ) {
;         _Float16* xr = X + (size_t)row * DM; f32x4 v[8], sum[8];
;         const int plc = pl[i]; unsigned long long sel = __ballot(plc >= 0);
; #pragma unroll
;         for (int j = 0; j < 8; ++j) { v[j] = __builtin_convertvector(nx[i][j], f32x4); sum[j] = (f32x4){0.f, 0.f, 0.f, 0.f}; }
;         { const int nrow = row + 4 * NGW;
;           if (nrow < SEQ) { pl[i] = (lane < NE) ? POS[(size_t)lane * SEQ + nrow] : -1;
; #pragma unroll
;             for (int j = 0; j < 8; ++j) nx[i][j] = *(const f16x4*)(X + (size_t)nrow * DM + ((j >> 1) * 512 + lane * 8 + (j & 1) * 4)); } }
;         while (sel) { const int e0 = __builtin_ctzll(sel); sel &= sel - 1;
;             const bf16_t* y0 = Y + (size_t)(e0 * CAP + __builtin_amdgcn_readlane(plc, e0)) * DM;
;             u32x2 w0[8];
; #pragma unroll
;             for (int j = 0; j < 8; ++j) w0[j] = *(const u32x2*)(y0 + ((j >> 1) * 512 + lane * 8 + (j & 1) * 4));
; #pragma unroll
;             for (int j = 0; j < 8; ++j) sum[j] += (f32x4){bflo(w0[j].x), bfhi(w0[j].x), bflo(w0[j].y), bfhi(w0[j].y)}; }
;         float ss = 0.f;
; #pragma unroll
;         for (int j = 0; j < 8; ++j) { const int c = ((j >> 1) * 512 + lane * 8 + (j & 1) * 4); v[j] = v[j] + *(const f32x4*)(gf + c) * sum[j];
;             ss += (v[j].x * v[j].x + v[j].y * v[j].y) + (v[j].z * v[j].z + v[j].w * v[j].w); }
.LBB0_2267:
	global_load_dwordx4 v[88:91], v[98:99], off
	global_load_dwordx4 v[84:87], v[98:99], off offset:16
	global_load_dwordx4 v[152:155], v[100:101], off
	global_load_dwordx4 v[156:159], v[100:101], off offset:16
	global_load_dwordx4 v[160:163], v[102:103], off
	global_load_dwordx4 v[164:167], v[102:103], off offset:16
	global_load_dwordx4 v[168:171], v[104:105], off offset:16
	global_load_dwordx4 v[172:175], v[104:105], off
	v_cvt_f32_f16_sdwa v185, v40 dst_sel:DWORD dst_unused:UNUSED_PAD src0_sel:WORD_1
	v_cvt_f32_f16_sdwa v187, v41 dst_sel:DWORD dst_unused:UNUSED_PAD src0_sel:WORD_1
	v_cvt_f32_f16_e32 v184, v40
	v_cvt_f32_f16_e32 v186, v41
	v_cvt_f32_f16_sdwa v41, v42 dst_sel:DWORD dst_unused:UNUSED_PAD src0_sel:WORD_1
	v_cvt_f32_f16_sdwa v189, v43 dst_sel:DWORD dst_unused:UNUSED_PAD src0_sel:WORD_1
	v_cvt_f32_f16_e32 v40, v42
	v_cvt_f32_f16_e32 v188, v43
	v_cvt_f32_f16_sdwa v43, v44 dst_sel:DWORD dst_unused:UNUSED_PAD src0_sel:WORD_1
	v_cvt_f32_f16_sdwa v191, v45 dst_sel:DWORD dst_unused:UNUSED_PAD src0_sel:WORD_1
	v_cvt_f32_f16_e32 v42, v44
	v_cvt_f32_f16_e32 v190, v45
	v_cvt_f32_f16_sdwa v45, v46 dst_sel:DWORD dst_unused:UNUSED_PAD src0_sel:WORD_1
	v_cvt_f32_f16_sdwa v193, v47 dst_sel:DWORD dst_unused:UNUSED_PAD src0_sel:WORD_1
	v_cvt_f32_f16_e32 v44, v46
	v_cvt_f32_f16_e32 v192, v47
	v_cvt_f32_f16_sdwa v47, v20 dst_sel:DWORD dst_unused:UNUSED_PAD src0_sel:WORD_1
	v_cvt_f32_f16_e32 v46, v20
	v_mov_b32_e32 v20, s19
	v_cvt_f32_f16_sdwa v177, v36 dst_sel:DWORD dst_unused:UNUSED_PAD src0_sel:WORD_1
	v_cvt_f32_f16_sdwa v179, v37 dst_sel:DWORD dst_unused:UNUSED_PAD src0_sel:WORD_1
	v_cvt_f32_f16_e32 v176, v36
	v_cvt_f32_f16_e32 v178, v37
	v_cvt_f32_f16_sdwa v181, v38 dst_sel:DWORD dst_unused:UNUSED_PAD src0_sel:WORD_1
	v_cvt_f32_f16_sdwa v183, v39 dst_sel:DWORD dst_unused:UNUSED_PAD src0_sel:WORD_1
	v_cvt_f32_f16_e32 v180, v38
	v_cvt_f32_f16_e32 v182, v39
	ds_read_b128 v[36:39], v20
	v_cvt_f32_f16_sdwa v195, v21 dst_sel:DWORD dst_unused:UNUSED_PAD src0_sel:WORD_1
	v_cvt_f32_f16_e32 v194, v21
	v_cvt_f32_f16_sdwa v197, v22 dst_sel:DWORD dst_unused:UNUSED_PAD src0_sel:WORD_1
	v_cvt_f32_f16_sdwa v199, v23 dst_sel:DWORD dst_unused:UNUSED_PAD src0_sel:WORD_1
	s_waitcnt lgkmcnt(0)
	v_readfirstlane_b32 s13, v37
	v_readfirstlane_b32 s12, v36
	v_cvt_f32_f16_e32 v196, v22
	v_cvt_f32_f16_e32 v198, v23
	s_ashr_i32 s11, s10, 31
	v_readfirstlane_b32 s9, v38
	v_readfirstlane_b32 s5, v39
	global_load_dwordx4 v[20:23], v149, s[12:13]
	s_waitcnt vmcnt(13)
	v_mov_b32_e32 v147, v150
	s_waitcnt vmcnt(8)
	v_pk_fma_f32 v[36:37], v[138:139], v[90:91], v[178:179]
	v_pk_fma_f32 v[88:89], v[136:137], v[88:89], v[176:177]
	s_waitcnt vmcnt(7)
	v_pk_fma_f32 v[86:87], v[134:135], v[86:87], v[182:183]
	v_pk_fma_f32 v[84:85], v[132:133], v[84:85], v[180:181]
	s_waitcnt vmcnt(6)
	v_pk_fma_f32 v[90:91], v[130:131], v[154:155], v[186:187]
	v_pk_fma_f32 v[128:129], v[128:129], v[152:153], v[184:185]
	s_waitcnt vmcnt(4)
	v_pk_fma_f32 v[42:43], v[120:121], v[160:161], v[42:43]
	s_waitcnt vmcnt(3)
	v_pk_fma_f32 v[44:45], v[116:117], v[164:165], v[44:45]
	v_mul_f32_e32 v116, v89, v89
	v_mul_f32_e32 v117, v37, v37
	v_mul_f32_e32 v120, v85, v85
	v_mul_f32_e32 v121, v87, v87
	v_pk_fma_f32 v[126:127], v[126:127], v[158:159], v[188:189]
	v_pk_fma_f32 v[40:41], v[124:125], v[156:157], v[40:41]
	v_mul_f32_e32 v124, v129, v129
	v_mul_f32_e32 v125, v91, v91
	v_fmac_f32_e32 v116, v88, v88
	v_fmac_f32_e32 v117, v36, v36
	v_fmac_f32_e32 v120, v84, v84
	v_fmac_f32_e32 v121, v86, v86
	v_pk_fma_f32 v[122:123], v[122:123], v[162:163], v[190:191]
	v_mul_f32_e32 v130, v41, v41
	v_mul_f32_e32 v131, v127, v127
	v_fmac_f32_e32 v124, v128, v128
	v_fmac_f32_e32 v125, v90, v90
	v_add_f32_e32 v116, v116, v117
	v_add_f32_e32 v117, v120, v121
	v_pk_fma_f32 v[118:119], v[118:119], v[166:167], v[192:193]
	v_mul_f32_e32 v132, v43, v43
	v_mul_f32_e32 v133, v123, v123
	v_fmac_f32_e32 v130, v40, v40
	v_fmac_f32_e32 v131, v126, v126
	v_add_f32_e32 v120, v124, v125
	v_add_f32_e32 v116, v116, v117
	v_mul_f32_e32 v134, v45, v45
	v_fmac_f32_e32 v132, v42, v42
	v_fmac_f32_e32 v133, v122, v122
	v_add_f32_e32 v121, v130, v131
	v_add_f32_e32 v116, v116, v120
	v_mul_f32_e32 v117, v119, v119
	s_waitcnt vmcnt(1)
; __device__ __forceinline__ unsigned f2bf(float f) { unsigned u = __builtin_bit_cast(unsigned, f); return (u + 0x7fffu + ((u >> 16) & 1u)) >> 16; }
; __device__ __forceinline__ void combine_phase(const Ctx& a, int layer, int G) {
;     ...
;         float ss = 0.f;
; #pragma unroll
;         for (int j = 0; j < 8; ++j) { const int c = ((j >> 1) * 512 + lane * 8 + (j & 1) * 4); v[j] = v[j] + *(const f32x4*)(gf + c) * sum[j];
;             ss += (v[j].x * v[j].x + v[j].y * v[j].y) + (v[j].z * v[j].z + v[j].w * v[j].w); }
;         const float rstd = 1.0f / sqrtf(wave_sum(ss) * (1.0f / DM) + EPS);
;         if (layer == 0) {
;             bf16_t* orow = (bf16_t*)(a.ws() + WS_HCAT) + (size_t)row * DM; const float* m1 = modl + 12288; const float* gain = a.g_mix() + DM;
;             float nyq[4] = {0.f, 0.f, 0.f, 0.f};
; #pragma unroll
;             for (int q = 0; q < 4; ++q) { const int c = q * 512 + lane * 8;
;                 { const f16x4 r0 = __builtin_convertvector(v[2 * q], f16x4), r1 = __builtin_convertvector(v[2 * q + 1], f16x4); *(f16x8*)(xr + c) = __builtin_shufflevector(r0, r1, 0, 1, 2, 3, 4, 5, 6, 7); }
;                 const f32x4 y0 = v[2 * q] * rstd * *(const f32x4*)(gain + c) * (1.0f + *(const f32x4*)(m1 + DM + c)) + *(const f32x4*)(m1 + c);
;                 const f32x4 y1 = v[2 * q + 1] * rstd * *(const f32x4*)(gain + c + 4) * (1.0f + *(const f32x4*)(m1 + DM + c + 4)) + *(const f32x4*)(m1 + c + 4);
;                 u32x4 w; w.x = pk2(y0.x, y0.y); w.y = pk2(y0.z, y0.w); w.z = pk2(y1.x, y1.y); w.w = pk2(y1.z, y1.w); *(u32x4*)(orow + c) = w;
;                 nyq[q] += ((bflo(w.x) - bfhi(w.x)) + (bflo(w.y) - bfhi(w.y))) + ((bflo(w.z) - bfhi(w.z)) + (bflo(w.w) - bfhi(w.w))); }
;             { bf16_t* WCT = (bf16_t*)(a.ws() + WS_WCT); const int n = (row & 127) * 64 + (row >> 7);
;                 float mine = 0.f;
; #pragma unroll
;                 for (int g = 0; g < 4; ++g) { const float sg = wave_sum(nyq[g]); mine = (lane == g) ? sg : mine; }
;                 if (lane < 4) { WCT[(size_t)(2048 + 2 * lane) * 8192 + n] = (bf16_t)f2bf(mine); WCT[(size_t)(2049 + 2 * lane) * 8192 + n] = 0; } }
;         } else {
;             float* orow = a.out() + (size_t)row * DM;
; #pragma unroll
;             for (int j = 0; j < 8; ++j) { const int c = ((j >> 1) * 512 + lane * 8 + (j & 1) * 4); *(f32x4*)(orow + c) = v[j] * rstd * *(const f32x4*)(a.g_final() + c); }
	v_pk_fma_f32 v[114:115], v[114:115], v[174:175], v[194:195]
	v_pk_fma_f32 v[46:47], v[112:113], v[172:173], v[46:47]
	v_fmac_f32_e32 v134, v44, v44
	v_add_f32_e32 v124, v132, v133
	v_add_f32_e32 v116, v116, v121
	v_fmac_f32_e32 v117, v118, v118
	v_mul_f32_e32 v112, v47, v47
	v_mul_f32_e32 v113, v115, v115
	v_add_f32_e32 v116, v116, v124
	v_add_f32_e32 v117, v134, v117
	v_fmac_f32_e32 v112, v46, v46
	v_fmac_f32_e32 v113, v114, v114
	v_add_f32_e32 v116, v116, v117
	v_add_f32_e32 v112, v112, v113
	v_pk_fma_f32 v[110:111], v[110:111], v[170:171], v[198:199]
	v_pk_fma_f32 v[108:109], v[108:109], v[168:169], v[196:197]
	v_add_f32_e32 v112, v116, v112
	v_mul_f32_e32 v113, v109, v109
	v_mul_f32_e32 v116, v111, v111
	v_fmac_f32_e32 v113, v108, v108
	v_fmac_f32_e32 v116, v110, v110
	v_add_f32_e32 v113, v113, v116
	v_add_f32_e32 v112, v112, v113
	s_nop 1
	v_add_f32_dpp v112, v112, v112 quad_perm:[1,0,3,2] row_mask:0xf bank_mask:0xf bound_ctrl:1
	s_nop 1
	v_add_f32_dpp v112, v112, v112 quad_perm:[2,3,0,1] row_mask:0xf bank_mask:0xf bound_ctrl:1
	s_nop 1
	v_add_f32_dpp v112, v112, v112 row_half_mirror row_mask:0xf bank_mask:0xf bound_ctrl:1
	s_nop 1
	v_add_f32_dpp v112, v112, v112 row_mirror row_mask:0xf bank_mask:0xf bound_ctrl:1
	v_mov_b32_e32 v113, v112
	s_nop 1
	v_permlane16_swap_b32_e32 v112, v113
	v_add_f32_e32 v112, v112, v113
	v_mov_b32_e32 v113, v112
	s_nop 1
	v_permlane32_swap_b32_e32 v112, v113
	v_add_f32_e32 v112, v112, v113
	v_fmamk_f32 v112, v112, 0x3a000000, v95
	v_mul_f32_e32 v113, 0x4f800000, v112
	v_cmp_gt_f32_e32 vcc, s21, v112
	s_nop 1
	v_cndmask_b32_e32 v112, v112, v113, vcc
	v_sqrt_f32_e32 v113, v112
	s_nop 0
	v_add_u32_e32 v116, -1, v113
	v_fma_f32 v117, -v116, v113, v112
	v_cmp_ge_f32_e64 s[2:3], 0, v117
	v_add_u32_e32 v117, 1, v113
	s_nop 0
	v_cndmask_b32_e64 v116, v113, v116, s[2:3]
	v_fma_f32 v113, -v117, v113, v112
	v_cmp_lt_f32_e64 s[2:3], 0, v113
	s_nop 1
	v_cndmask_b32_e64 v113, v116, v117, s[2:3]
	v_mul_f32_e32 v116, 0x37800000, v113
	v_cndmask_b32_e32 v113, v113, v116, vcc
	v_cmp_class_f32_e32 vcc, v112, v140
	s_nop 1
	v_cndmask_b32_e32 v112, v113, v112, vcc
	v_div_scale_f32 v113, s[2:3], v112, v112, 1.0
	v_rcp_f32_e32 v116, v113
	s_lshl_b64 s[2:3], s[10:11], 13
	s_add_u32 s2, s9, s2
	s_addc_u32 s3, s5, s3
	v_fma_f32 v117, -v113, v116, 1.0
	v_fmac_f32_e32 v116, v117, v116
	v_div_scale_f32 v117, vcc, 1.0, v112, 1.0
	v_mul_f32_e32 v120, v117, v116
	v_fma_f32 v121, -v113, v120, v117
	v_fmac_f32_e32 v120, v121, v116
	v_fma_f32 v113, -v113, v120, v117
	v_div_fmas_f32 v113, v113, v116, v120
	v_div_fixup_f32 v112, v113, v112, 1.0
	v_pk_mul_f32 v[38:39], v[88:89], v[112:113] op_sel_hi:[1,0]
	v_pk_mul_f32 v[36:37], v[36:37], v[112:113] op_sel_hi:[1,0]
	s_waitcnt vmcnt(0)
	v_pk_mul_f32 v[20:21], v[20:21], v[38:39]
	v_pk_mul_f32 v[22:23], v[22:23], v[36:37]
	global_store_dwordx4 v149, v[20:23], s[2:3]
	v_pk_mul_f32 v[36:37], v[86:87], v[112:113] op_sel_hi:[1,0]
	v_pk_mul_f32 v[38:39], v[84:85], v[112:113] op_sel_hi:[1,0]
	v_pk_mul_f32 v[22:23], v[222:223], v[36:37]
	v_pk_mul_f32 v[20:21], v[220:221], v[38:39]
	global_store_dwordx4 v149, v[20:23], s[2:3] offset:16
	v_pk_mul_f32 v[36:37], v[90:91], v[112:113] op_sel_hi:[1,0]
	v_pk_mul_f32 v[38:39], v[128:129], v[112:113] op_sel_hi:[1,0]
	v_pk_mul_f32 v[22:23], v[226:227], v[36:37]
	v_pk_mul_f32 v[20:21], v[224:225], v[38:39]
	global_store_dwordx4 v149, v[20:23], s[2:3] offset:2048
	v_pk_mul_f32 v[36:37], v[126:127], v[112:113] op_sel_hi:[1,0]
	v_pk_mul_f32 v[38:39], v[40:41], v[112:113] op_sel_hi:[1,0]
	v_mov_b64_e32 v[40:41], v[72:73]
	v_pk_mul_f32 v[20:21], v[38:39], v[228:229]
	v_pk_mul_f32 v[22:23], v[36:37], v[230:231]
	global_store_dwordx4 v149, v[20:23], s[2:3] offset:2064
	v_pk_mul_f32 v[36:37], v[122:123], v[112:113] op_sel_hi:[1,0]
	v_pk_mul_f32 v[38:39], v[42:43], v[112:113] op_sel_hi:[1,0]
	v_mov_b64_e32 v[42:43], v[74:75]
	v_pk_mul_f32 v[20:21], v[38:39], v[232:233]
	v_pk_mul_f32 v[22:23], v[36:37], v[234:235]
	global_store_dwordx4 v141, v[20:23], s[2:3]
	v_pk_mul_f32 v[36:37], v[118:119], v[112:113] op_sel_hi:[1,0]
	v_pk_mul_f32 v[38:39], v[44:45], v[112:113] op_sel_hi:[1,0]
	v_mov_b64_e32 v[44:45], v[76:77]
	v_pk_mul_f32 v[20:21], v[38:39], v[236:237]
	v_pk_mul_f32 v[22:23], v[36:37], v[238:239]
	global_store_dwordx4 v142, v[20:23], s[2:3]
	v_pk_mul_f32 v[36:37], v[114:115], v[112:113] op_sel_hi:[1,0]
	v_pk_mul_f32 v[38:39], v[46:47], v[112:113] op_sel_hi:[1,0]
	v_mov_b64_e32 v[46:47], v[78:79]
	v_pk_mul_f32 v[20:21], v[38:39], v[240:241]
	v_pk_mul_f32 v[22:23], v[36:37], v[242:243]
	global_store_dwordx4 v143, v[20:23], s[2:3]
	v_mov_b64_e32 v[36:37], v[68:69]
	v_mov_b64_e32 v[38:39], v[70:71]
	v_pk_mul_f32 v[70:71], v[110:111], v[112:113] op_sel_hi:[1,0]
	v_pk_mul_f32 v[68:69], v[108:109], v[112:113] op_sel_hi:[1,0]
	v_mov_b64_e32 v[20:21], v[80:81]
	v_mov_b64_e32 v[22:23], v[82:83]
	v_pk_mul_f32 v[68:69], v[68:69], v[244:245]
	v_pk_mul_f32 v[70:71], v[70:71], v[246:247]
	global_store_dwordx4 v144, v[68:71], s[2:3]
	s_add_i32 s8, s8, s16
	s_cmpk_gt_i32 s8, 0x1fff
	s_cbranch_scc1 .LBB0_2238

; __global__ void __launch_bounds__(NTHR, 2) fwd(Args ka) {
	.amdhsa_kernel _Z3fwd4Args
		.amdhsa_group_segment_fixed_size 0
		.amdhsa_private_segment_fixed_size 0
		.amdhsa_kernarg_size 480
		.amdhsa_user_sgpr_count 2
		.amdhsa_user_sgpr_dispatch_ptr 0
		.amdhsa_user_sgpr_queue_ptr 0
		.amdhsa_user_sgpr_kernarg_segment_ptr 1
		.amdhsa_user_sgpr_dispatch_id 0
		.amdhsa_user_sgpr_kernarg_preload_length 0
		.amdhsa_user_sgpr_kernarg_preload_offset 0
		.amdhsa_user_sgpr_private_segment_size 0
		.amdhsa_uses_dynamic_stack 0
		.amdhsa_enable_private_segment 0
		.amdhsa_system_sgpr_workgroup_id_x 1
		.amdhsa_system_sgpr_workgroup_id_y 0
		.amdhsa_system_sgpr_workgroup_id_z 0
		.amdhsa_system_sgpr_workgroup_info 0
		.amdhsa_system_vgpr_workitem_id 0
		.amdhsa_next_free_vgpr 249
		.amdhsa_next_free_sgpr 102
		.amdhsa_accum_offset 252
		.amdhsa_reserve_vcc 1
		.amdhsa_float_round_mode_32 0
		.amdhsa_float_round_mode_16_64 0
		.amdhsa_float_denorm_mode_32 3
		.amdhsa_float_denorm_mode_16_64 3
		.amdhsa_dx10_clamp 1
		.amdhsa_ieee_mode 1
		.amdhsa_fp16_overflow 0
		.amdhsa_tg_split 0
		.amdhsa_exception_fp_ieee_invalid_op 0
		.amdhsa_exception_fp_denorm_src 0
		.amdhsa_exception_fp_ieee_div_zero 0
		.amdhsa_exception_fp_ieee_overflow 0
		.amdhsa_exception_fp_ieee_underflow 0
		.amdhsa_exception_fp_ieee_inexact 0
		.amdhsa_exception_int_div_zero 0
	.end_amdhsa_kernel

; __global__ void __launch_bounds__(NTHR, 2) fwd(Args ka) {
amdhsa.kernels:
  - .agpr_count:     0
    .args:
      - .offset:         0
        .size:           224
        .value_kind:     by_value
      - .offset:         224
        .size:           4
        .value_kind:     hidden_block_count_x
      - .offset:         228
        .size:           4
        .value_kind:     hidden_block_count_y
      - .offset:         232
        .size:           4
        .value_kind:     hidden_block_count_z
      - .offset:         236
        .size:           2
        .value_kind:     hidden_group_size_x
      - .offset:         238
        .size:           2
        .value_kind:     hidden_group_size_y
      - .offset:         240
        .size:           2
        .value_kind:     hidden_group_size_z
      - .offset:         242
        .size:           2
        .value_kind:     hidden_remainder_x
      - .offset:         244
        .size:           2
        .value_kind:     hidden_remainder_y
      - .offset:         246
        .size:           2
        .value_kind:     hidden_remainder_z
      - .offset:         264
        .size:           8
        .value_kind:     hidden_global_offset_x
      - .offset:         272
        .size:           8
        .value_kind:     hidden_global_offset_y
      - .offset:         280
        .size:           8
        .value_kind:     hidden_global_offset_z
      - .offset:         288
        .size:           2
        .value_kind:     hidden_grid_dims
      - .offset:         344
        .size:           4
        .value_kind:     hidden_dynamic_lds_size
    .group_segment_fixed_size: 0
    .kernarg_segment_align: 8
    .kernarg_segment_size: 480
    .language:       OpenCL C
    .language_version:
      - 2
      - 0
    .max_flat_workgroup_size: 512
    .name:           _Z3fwd4Args
    .private_segment_fixed_size: 0
    .sgpr_count:     108
    .sgpr_spill_count: 25
    .symbol:         _Z3fwd4Args.kd
    .uniform_work_group_size: 1
    .uses_dynamic_stack: false
    .vgpr_count:     249
    .vgpr_spill_count: 0
    .wavefront_size: 64
